# baseline (speedup 1.0000x reference)
.LBB3_28:
	v_add_u32_e32 v8, 0xc00, v4
	ds_read2_b32 v[6:7], v4 offset1:100
	v_add_u32_e32 v10, 0x200, v4
	v_add_u32_e32 v16, 0x800, v4
	v_add_u32_e32 v13, 0x400, v4
	ds_read2_b32 v[8:9], v8 offset0:32 offset1:132
	ds_read2_b32 v[10:11], v10 offset0:72 offset1:172
	ds_read2_b32 v[14:15], v13 offset0:144 offset1:244
	ds_read2_b32 v[16:17], v16 offset0:88 offset1:188
	s_waitcnt vmcnt(0) lgkmcnt(0)
	v_fmac_f32_e32 v9, v19, v6
	v_mul_f32_e32 v6, v20, v7
	v_add_f32_e32 v9, v9, v6
	v_mul_f32_e32 v6, v21, v10
	v_add_f32_e32 v9, v9, v6
	v_mul_f32_e32 v6, v22, v11
	v_add_f32_e32 v9, v9, v6
	v_mul_f32_e32 v6, v23, v14
	v_add_f32_e32 v9, v9, v6
	v_mul_f32_e32 v6, v24, v15
	v_add_f32_e32 v9, v9, v6
	v_mul_f32_e32 v6, v25, v16
	v_add_f32_e32 v9, v9, v6
	v_mul_f32_e32 v6, v26, v17
	v_add_f32_e32 v9, v9, v6
	v_mul_f32_e32 v6, v27, v8
	v_add_u32_e32 v2, 1, v2
	v_add_f32_e32 v6, v9, v6
	v_cmp_ge_u32_e64 s[2:3], v2, v3
	v_max_f32_e32 v6, 0, v6
	v_add_u32_e32 v4, 4, v4
	s_or_b64 s[6:7], s[2:3], s[6:7]
	ds_write_b32 v5, v6
	v_add_u32_e32 v5, 0x100, v5
	s_andn2_b64 exec, exec, s[6:7]
	s_cbranch_execnz .LBB3_28
	s_or_b64 exec, exec, s[6:7]
